# attention tile loops: cross-lane row max via v_permlane16/32_swap instead of four serialized ds_bpermute round trips
# speedup vs baseline: 1.0066x; 1.0066x over previous
.LBB0_395:
	v_add_u32_e32 v147, s88, v149
	v_mov_b32_e32 v109, v180
	v_add_u32_e32 v180, v147, v151
	ds_read_b128 v[188:191], v180 offset:0
	v_mov_b32_e32 v110, v181
	v_add_u32_e32 v181, v147, v182
	ds_read_b128 v[218:221], v181 offset:0
	v_add_u32_e32 v187, v147, v183
	ds_read_b128 v[222:225], v187 offset:0
	s_waitcnt lgkmcnt(2)
	v_add_u32_e32 v147, v147, v184
	v_mfma_f32_16x16x32_bf16 v[108:111], v[188:191], v[38:41], v[108:111]
	v_mfma_f32_16x16x32_bf16 v[112:115], v[188:191], v[54:57], v[112:115]
	ds_read_b128 v[188:191], v147 offset:0
	s_waitcnt lgkmcnt(2)
	v_mfma_f32_16x16x32_bf16 v[108:111], v[218:221], v[42:45], v[108:111]
	v_mfma_f32_16x16x32_bf16 v[112:115], v[218:221], v[58:61], v[112:115]
	ds_read_b128 v[218:221], v180 offset:0x1000
	s_waitcnt lgkmcnt(2)
	v_mfma_f32_16x16x32_bf16 v[108:111], v[222:225], v[46:49], v[108:111]
	ds_read_b128 v[226:229], v181 offset:0x1000
	s_waitcnt lgkmcnt(2)
	v_mfma_f32_16x16x32_bf16 v[222:225], v[222:225], v[62:65], v[112:115]
	v_mfma_f32_16x16x32_bf16 v[112:115], v[188:191], v[50:53], v[108:111]
	v_mfma_f32_16x16x32_bf16 v[108:111], v[188:191], v[66:69], v[222:225]
	ds_read_b128 v[188:191], v187 offset:0x1000
	s_waitcnt lgkmcnt(2)
	v_mfma_f32_16x16x32_bf16 v[116:119], v[218:221], v[38:41], v[116:119]
	v_mfma_f32_16x16x32_bf16 v[120:123], v[218:221], v[54:57], v[120:123]
	ds_read_b128 v[218:221], v147 offset:0x1000
	s_waitcnt lgkmcnt(2)
	v_mfma_f32_16x16x32_bf16 v[116:119], v[226:229], v[42:45], v[116:119]
	ds_read_b128 v[222:225], v180 offset:0x2000
	s_waitcnt lgkmcnt(2)
	v_mfma_f32_16x16x32_bf16 v[120:123], v[226:229], v[58:61], v[120:123]
	v_mfma_f32_16x16x32_bf16 v[116:119], v[188:191], v[46:49], v[116:119]
	ds_read_b128 v[226:229], v181 offset:0x2000
	s_waitcnt lgkmcnt(2)
	v_mfma_f32_16x16x32_bf16 v[188:191], v[188:191], v[62:65], v[120:123]
	v_mfma_f32_16x16x32_bf16 v[120:123], v[218:221], v[50:53], v[116:119]
	v_mfma_f32_16x16x32_bf16 v[116:119], v[218:221], v[66:69], v[188:191]
	ds_read_b128 v[188:191], v187 offset:0x2000
	s_waitcnt lgkmcnt(2)
	v_mfma_f32_16x16x32_bf16 v[124:127], v[222:225], v[38:41], v[124:127]
	ds_read_b128 v[218:221], v147 offset:0x2000
	s_waitcnt lgkmcnt(2)
	v_mfma_f32_16x16x32_bf16 v[132:135], v[222:225], v[54:57], v[132:135]
	v_mfma_f32_16x16x32_bf16 v[124:127], v[226:229], v[42:45], v[124:127]
	ds_read_b128 v[222:225], v180 offset:0x3000
	s_waitcnt lgkmcnt(2)
	v_mfma_f32_16x16x32_bf16 v[132:135], v[226:229], v[58:61], v[132:135]
	s_nop 1
	v_mfma_f32_16x16x32_bf16 v[124:127], v[188:191], v[46:49], v[124:127]
	ds_read_b128 v[226:229], v181 offset:0x3000
	s_waitcnt lgkmcnt(2)
	v_mfma_f32_16x16x32_bf16 v[188:191], v[188:191], v[62:65], v[132:135]
	v_mfma_f32_16x16x32_bf16 v[132:135], v[218:221], v[50:53], v[124:127]
	v_mfma_f32_16x16x32_bf16 v[124:127], v[218:221], v[66:69], v[188:191]
	ds_read_b128 v[188:191], v187 offset:0x3000
	s_waitcnt lgkmcnt(2)
	v_mfma_f32_16x16x32_bf16 v[128:131], v[222:225], v[38:41], v[128:131]
	ds_read_b128 v[218:221], v147 offset:0x3000
	s_waitcnt lgkmcnt(2)
	v_mfma_f32_16x16x32_bf16 v[136:139], v[222:225], v[54:57], v[136:139]
	v_mfma_f32_16x16x32_bf16 v[128:131], v[226:229], v[42:45], v[128:131]
	s_waitcnt lgkmcnt(1)
	v_mfma_f32_16x16x32_bf16 v[136:139], v[226:229], v[58:61], v[136:139]
	s_nop 1
	v_mfma_f32_16x16x32_bf16 v[128:131], v[188:191], v[46:49], v[128:131]
	s_waitcnt lgkmcnt(0)
	v_mfma_f32_16x16x32_bf16 v[188:191], v[188:191], v[62:65], v[136:139]
	v_and_b32_e32 v180, 64, v208
	v_xor_b32_e32 v147, 16, v208
	v_add_u32_e32 v180, 64, v180
	v_cmp_lt_i32_e32 vcc, v147, v180
	v_mfma_f32_16x16x32_bf16 v[136:139], v[218:221], v[50:53], v[128:131]
	s_mov_b64 s[0:1], 0
	v_cndmask_b32_e32 v147, v208, v147, vcc
	v_lshlrev_b32_e32 v181, 2, v147
	v_xor_b32_e32 v147, 32, v208
	v_cmp_lt_i32_e32 vcc, v147, v180
	v_mfma_f32_16x16x32_bf16 v[128:131], v[218:221], v[66:69], v[188:191]
	s_mov_b64 s[54:55], 0
	v_cndmask_b32_e32 v147, v208, v147, vcc
	v_lshlrev_b32_e32 v187, 2, v147
	v_max3_f32 v147, v112, s30, v113
	v_max3_f32 v147, v147, v114, v115
	v_max3_f32 v147, v147, v120, v121
	v_max3_f32 v147, v147, v122, v123
	v_max3_f32 v147, v147, v132, v133
	v_max3_f32 v147, v147, v134, v135
	v_max3_f32 v147, v147, v136, v137
	v_max3_f32 v147, v147, v138, v139
	v_max3_f32 v180, v108, s30, v109
	v_max3_f32 v180, v180, v110, v111
	v_max3_f32 v180, v180, v116, v117
	v_max3_f32 v180, v180, v118, v119
	v_max3_f32 v180, v180, v124, v125
	v_max3_f32 v180, v180, v126, v127
	v_max3_f32 v180, v180, v128, v129
	v_max3_f32 v180, v180, v130, v131
	v_mov_b32_e32 v230, v147
	v_mov_b32_e32 v231, v180
	s_nop 1
	v_permlane16_swap_b32 v230, v147
	v_permlane16_swap_b32 v231, v180
	v_max_f32_e32 v147, v147, v230
	v_max_f32_e32 v180, v180, v231
	v_mov_b32_e32 v230, v147
	v_mov_b32_e32 v231, v180
	s_nop 1
	v_permlane32_swap_b32 v230, v147
	v_permlane32_swap_b32 v231, v180
	v_max_f32_e32 v147, v147, v230
	v_max_f32_e32 v180, v180, v231
	v_cmp_lt_f32_e32 vcc, s31, v147
	s_and_saveexec_b64 s[56:57], vcc
	v_cmp_lt_f32_e32 vcc, s34, v147
	s_xor_b64 s[54:55], s[52:53], -1
	s_or_b64 s[54:55], vcc, s[54:55]
	s_and_b64 s[54:55], s[54:55], exec
	s_or_b64 exec, exec, s[56:57]
	v_cmp_lt_f32_e32 vcc, s31, v180
	s_and_saveexec_b64 s[56:57], vcc
	v_cmp_lt_f32_e32 vcc, s34, v180
	s_xor_b64 s[0:1], s[48:49], -1
	s_or_b64 s[0:1], vcc, s[0:1]
	s_and_b64 s[0:1], s[0:1], exec
	s_or_b64 exec, exec, s[56:57]
	s_or_b64 s[56:57], s[54:55], s[0:1]
	v_cndmask_b32_e64 v181, 0, 1, s[56:57]
	v_cmp_ne_u32_e32 vcc, 0, v181
	s_cbranch_vccz .LBB0_401
	v_cndmask_b32_e64 v188, 0, v180, s[0:1]
	v_cndmask_b32_e64 v147, 0, v147, s[54:55]
	v_exp_f32_e64 v180, -v188
	v_exp_f32_e64 v187, -v147
	s_and_b64 vcc, s[0:1], s[48:49]
	s_or_b64 s[0:1], s[48:49], s[0:1]
	v_cndmask_b32_e32 v181, 1.0, v180, vcc
	s_and_b64 vcc, s[54:55], s[52:53]
	v_cndmask_b32_e32 v180, 1.0, v187, vcc
	s_or_b64 s[54:55], s[52:53], s[54:55]
	v_pk_mul_f32 v[100:101], v[100:101], v[180:181] op_sel_hi:[1,0]
	v_pk_mul_f32 v[98:99], v[98:99], v[180:181] op_sel_hi:[1,0]
	v_pk_mul_f32 v[96:97], v[96:97], v[180:181] op_sel_hi:[1,0]
	v_pk_mul_f32 v[94:95], v[94:95], v[180:181] op_sel_hi:[1,0]
	v_pk_mul_f32 v[92:93], v[92:93], v[180:181] op_sel_hi:[1,0]
	v_pk_mul_f32 v[90:91], v[90:91], v[180:181] op_sel_hi:[1,0]
	v_pk_mul_f32 v[88:89], v[88:89], v[180:181] op_sel_hi:[1,0]
	v_pk_mul_f32 v[86:87], v[86:87], v[180:181] op_sel_hi:[1,0]
	v_pk_mul_f32 v[84:85], v[84:85], v[180:181] op_sel_hi:[1,0]
	v_pk_mul_f32 v[82:83], v[82:83], v[180:181] op_sel_hi:[1,0]
	v_pk_mul_f32 v[80:81], v[80:81], v[180:181] op_sel_hi:[1,0]
	v_pk_mul_f32 v[78:79], v[78:79], v[180:181] op_sel_hi:[1,0]
	v_pk_mul_f32 v[76:77], v[76:77], v[180:181] op_sel_hi:[1,0]
	v_pk_mul_f32 v[74:75], v[74:75], v[180:181] op_sel_hi:[1,0]
	v_pk_mul_f32 v[72:73], v[72:73], v[180:181] op_sel_hi:[1,0]
	v_pk_mul_f32 v[70:71], v[70:71], v[180:181] op_sel_hi:[1,0]
	v_pk_mul_f32 v[152:153], v[152:153], v[180:181]
	v_mov_b32_e32 v180, v181
	s_andn2_b64 s[52:53], s[52:53], exec
	s_and_b64 s[54:55], s[54:55], exec
	s_andn2_b64 s[48:49], s[48:49], exec
	s_and_b64 s[0:1], s[0:1], exec
	v_add_f32_e32 v146, v146, v147
	v_sub_f32_e32 v112, v112, v147
	v_sub_f32_e32 v113, v113, v147
	v_sub_f32_e32 v114, v114, v147
	v_sub_f32_e32 v115, v115, v147
	v_sub_f32_e32 v120, v120, v147
	v_sub_f32_e32 v121, v121, v147
	v_sub_f32_e32 v122, v122, v147
	v_sub_f32_e32 v123, v123, v147
	v_sub_f32_e32 v132, v132, v147
	v_sub_f32_e32 v133, v133, v147
	v_sub_f32_e32 v134, v134, v147
	v_sub_f32_e32 v135, v135, v147
	v_sub_f32_e32 v136, v136, v147
	v_sub_f32_e32 v137, v137, v147
	v_sub_f32_e32 v138, v138, v147
	v_sub_f32_e32 v139, v139, v147
	v_add_f32_e32 v2, v2, v188
	v_pk_mul_f32 v[36:37], v[36:37], v[180:181] op_sel_hi:[1,0]
	v_pk_mul_f32 v[34:35], v[34:35], v[180:181] op_sel_hi:[1,0]
	v_pk_mul_f32 v[32:33], v[32:33], v[180:181] op_sel_hi:[1,0]
	v_pk_mul_f32 v[30:31], v[30:31], v[180:181] op_sel_hi:[1,0]
	v_pk_mul_f32 v[28:29], v[28:29], v[180:181] op_sel_hi:[1,0]
	v_pk_mul_f32 v[26:27], v[26:27], v[180:181] op_sel_hi:[1,0]
	v_pk_mul_f32 v[20:21], v[20:21], v[180:181] op_sel_hi:[1,0]
	v_pk_mul_f32 v[18:19], v[18:19], v[180:181] op_sel_hi:[1,0]
	v_pk_mul_f32 v[24:25], v[24:25], v[180:181] op_sel_hi:[1,0]
	v_pk_mul_f32 v[22:23], v[22:23], v[180:181] op_sel_hi:[1,0]
	v_pk_mul_f32 v[16:17], v[16:17], v[180:181] op_sel_hi:[1,0]
	v_pk_mul_f32 v[14:15], v[14:15], v[180:181] op_sel_hi:[1,0]
	v_pk_mul_f32 v[12:13], v[12:13], v[180:181] op_sel_hi:[1,0]
	v_pk_mul_f32 v[10:11], v[10:11], v[180:181] op_sel_hi:[1,0]
	v_pk_mul_f32 v[8:9], v[8:9], v[180:181] op_sel_hi:[1,0]
	v_pk_mul_f32 v[6:7], v[6:7], v[180:181] op_sel_hi:[1,0]
	v_sub_f32_e32 v108, v108, v188
	v_sub_f32_e32 v109, v109, v188
	v_sub_f32_e32 v110, v110, v188
	v_sub_f32_e32 v111, v111, v188
	v_sub_f32_e32 v116, v116, v188
	v_sub_f32_e32 v117, v117, v188
	v_sub_f32_e32 v118, v118, v188
	v_sub_f32_e32 v119, v119, v188
	v_sub_f32_e32 v124, v124, v188
	v_sub_f32_e32 v125, v125, v188
	v_sub_f32_e32 v126, v126, v188
	v_sub_f32_e32 v127, v127, v188
	v_sub_f32_e32 v128, v128, v188
	v_sub_f32_e32 v129, v129, v188
	v_sub_f32_e32 v130, v130, v188
	v_sub_f32_e32 v131, v131, v188
	s_or_b64 s[52:53], s[52:53], s[54:55]
	s_or_b64 s[48:49], s[48:49], s[0:1]

.LBB0_420:
	v_add_u32_e32 v158, s67, v161
	v_add_u32_e32 v160, v158, v162
	ds_read_b128 v[170:173], v160 offset:0
	v_add_u32_e32 v169, v158, v163
	ds_read_b128 v[174:177], v169 offset:0
	v_add_u32_e32 v186, v158, v164
	ds_read_b128 v[178:181], v186 offset:0
	s_waitcnt lgkmcnt(2)
	v_add_u32_e32 v158, v158, v165
	v_mfma_f32_16x16x32_bf16 v[106:109], v[170:173], v[30:33], v[106:109]
	v_mfma_f32_16x16x32_bf16 v[110:113], v[170:173], v[50:53], v[110:113]
	ds_read_b128 v[170:173], v158 offset:0
	s_waitcnt lgkmcnt(2)
	v_mfma_f32_16x16x32_bf16 v[106:109], v[174:177], v[34:37], v[106:109]
	v_mfma_f32_16x16x32_bf16 v[110:113], v[174:177], v[54:57], v[110:113]
	ds_read_b128 v[174:177], v160 offset:0x1000
	s_waitcnt lgkmcnt(2)
	v_mfma_f32_16x16x32_bf16 v[106:109], v[178:181], v[38:41], v[106:109]
	ds_read_b128 v[182:185], v169 offset:0x1000
	s_waitcnt lgkmcnt(2)
	v_mfma_f32_16x16x32_bf16 v[178:181], v[178:181], v[58:61], v[110:113]
	v_mfma_f32_16x16x32_bf16 v[110:113], v[170:173], v[46:49], v[106:109]
	v_mfma_f32_16x16x32_bf16 v[106:109], v[170:173], v[62:65], v[178:181]
	ds_read_b128 v[170:173], v186 offset:0x1000
	s_waitcnt lgkmcnt(2)
	v_mfma_f32_16x16x32_bf16 v[114:117], v[174:177], v[30:33], v[114:117]
	v_mfma_f32_16x16x32_bf16 v[118:121], v[174:177], v[50:53], v[118:121]
	ds_read_b128 v[174:177], v158 offset:0x1000
	s_waitcnt lgkmcnt(2)
	v_mfma_f32_16x16x32_bf16 v[114:117], v[182:185], v[34:37], v[114:117]
	ds_read_b128 v[178:181], v160 offset:0x2000
	s_waitcnt lgkmcnt(2)
	v_mfma_f32_16x16x32_bf16 v[118:121], v[182:185], v[54:57], v[118:121]
	v_mfma_f32_16x16x32_bf16 v[114:117], v[170:173], v[38:41], v[114:117]
	ds_read_b128 v[182:185], v169 offset:0x2000
	s_waitcnt lgkmcnt(2)
	v_mfma_f32_16x16x32_bf16 v[170:173], v[170:173], v[58:61], v[118:121]
	v_mfma_f32_16x16x32_bf16 v[118:121], v[174:177], v[46:49], v[114:117]
	v_mfma_f32_16x16x32_bf16 v[114:117], v[174:177], v[62:65], v[170:173]
	ds_read_b128 v[170:173], v186 offset:0x2000
	s_waitcnt lgkmcnt(2)
	v_mfma_f32_16x16x32_bf16 v[122:125], v[178:181], v[30:33], v[122:125]
	ds_read_b128 v[174:177], v158 offset:0x2000
	s_waitcnt lgkmcnt(2)
	v_mfma_f32_16x16x32_bf16 v[130:133], v[178:181], v[50:53], v[130:133]
	v_mfma_f32_16x16x32_bf16 v[122:125], v[182:185], v[34:37], v[122:125]
	ds_read_b128 v[178:181], v160 offset:0x3000
	s_waitcnt lgkmcnt(2)
	v_mfma_f32_16x16x32_bf16 v[130:133], v[182:185], v[54:57], v[130:133]
	s_nop 1
	v_mfma_f32_16x16x32_bf16 v[122:125], v[170:173], v[38:41], v[122:125]
	ds_read_b128 v[182:185], v169 offset:0x3000
	s_waitcnt lgkmcnt(2)
	v_mfma_f32_16x16x32_bf16 v[170:173], v[170:173], v[58:61], v[130:133]
	v_mfma_f32_16x16x32_bf16 v[130:133], v[174:177], v[46:49], v[122:125]
	v_mfma_f32_16x16x32_bf16 v[122:125], v[174:177], v[62:65], v[170:173]
	ds_read_b128 v[170:173], v186 offset:0x3000
	s_waitcnt lgkmcnt(2)
	v_mfma_f32_16x16x32_bf16 v[126:129], v[178:181], v[30:33], v[126:129]
	ds_read_b128 v[174:177], v158 offset:0x3000
	s_waitcnt lgkmcnt(2)
	v_mfma_f32_16x16x32_bf16 v[134:137], v[178:181], v[50:53], v[134:137]
	v_mfma_f32_16x16x32_bf16 v[126:129], v[182:185], v[34:37], v[126:129]
	s_waitcnt lgkmcnt(1)
	v_mfma_f32_16x16x32_bf16 v[134:137], v[182:185], v[54:57], v[134:137]
	s_nop 1
	v_mfma_f32_16x16x32_bf16 v[126:129], v[170:173], v[38:41], v[126:129]
	s_waitcnt lgkmcnt(0)
	v_mfma_f32_16x16x32_bf16 v[170:173], v[170:173], v[58:61], v[134:137]
	v_and_b32_e32 v160, 64, v208
	v_xor_b32_e32 v158, 16, v208
	v_add_u32_e32 v160, 64, v160
	v_cmp_lt_i32_e32 vcc, v158, v160
	v_mfma_f32_16x16x32_bf16 v[134:137], v[174:177], v[46:49], v[126:129]
	s_mov_b64 s[48:49], 0
	v_cndmask_b32_e32 v158, v208, v158, vcc
	v_lshlrev_b32_e32 v169, 2, v158
	v_xor_b32_e32 v158, 32, v208
	v_cmp_lt_i32_e32 vcc, v158, v160
	v_mfma_f32_16x16x32_bf16 v[126:129], v[174:177], v[62:65], v[170:173]
	s_mov_b64 s[52:53], 0
	v_cndmask_b32_e32 v158, v208, v158, vcc
	s_nop 0
	v_lshlrev_b32_e32 v170, 2, v158
	v_max3_f32 v158, v110, s30, v111
	v_max3_f32 v158, v158, v112, v113
	v_max3_f32 v158, v158, v118, v119
	v_max3_f32 v158, v158, v120, v121
	v_max3_f32 v158, v158, v130, v131
	v_max3_f32 v158, v158, v132, v133
	v_max3_f32 v158, v158, v134, v135
	v_max3_f32 v158, v158, v136, v137
	v_max3_f32 v160, v106, s30, v107
	v_max3_f32 v160, v160, v108, v109
	v_max3_f32 v160, v160, v114, v115
	v_max3_f32 v160, v160, v116, v117
	v_max3_f32 v160, v160, v122, v123
	v_max3_f32 v160, v160, v124, v125
	v_max3_f32 v160, v160, v126, v127
	v_max3_f32 v160, v160, v128, v129
	v_mov_b32_e32 v230, v158
	v_mov_b32_e32 v231, v160
	s_nop 1
	v_permlane16_swap_b32 v230, v158
	v_permlane16_swap_b32 v231, v160
	v_max_f32_e32 v158, v158, v230
	v_max_f32_e32 v160, v160, v231
	v_mov_b32_e32 v230, v158
	v_mov_b32_e32 v231, v160
	s_nop 1
	v_permlane32_swap_b32 v230, v158
	v_permlane32_swap_b32 v231, v160
	v_max_f32_e32 v158, v158, v230
	v_max_f32_e32 v160, v160, v231
	v_cmp_lt_f32_e32 vcc, s31, v158
	s_and_saveexec_b64 s[54:55], vcc
	v_cmp_lt_f32_e32 vcc, s34, v158
	s_xor_b64 s[52:53], s[46:47], -1
	s_or_b64 s[52:53], vcc, s[52:53]
	s_and_b64 s[52:53], s[52:53], exec
	s_or_b64 exec, exec, s[54:55]
	v_cmp_lt_f32_e32 vcc, s31, v160
	s_and_saveexec_b64 s[54:55], vcc
	v_cmp_lt_f32_e32 vcc, s34, v160
	s_xor_b64 s[48:49], s[44:45], -1
	s_or_b64 s[48:49], vcc, s[48:49]
	s_and_b64 s[48:49], s[48:49], exec
	s_or_b64 exec, exec, s[54:55]
	s_or_b64 s[54:55], s[52:53], s[48:49]
	v_cndmask_b32_e64 v169, 0, 1, s[54:55]
	v_cmp_ne_u32_e32 vcc, 0, v169
	s_cbranch_vccz .LBB0_413
	v_cndmask_b32_e64 v160, 0, v160, s[48:49]
	v_cndmask_b32_e64 v158, 0, v158, s[52:53]
	v_exp_f32_e64 v170, -v160
	v_exp_f32_e64 v169, -v158
	s_and_b64 vcc, s[48:49], s[44:45]
	s_or_b64 s[48:49], s[44:45], s[48:49]
	v_cndmask_b32_e32 v171, 1.0, v170, vcc
	s_and_b64 vcc, s[52:53], s[46:47]
	s_or_b64 s[52:53], s[46:47], s[52:53]
	v_add_f32_e32 v167, v167, v158
	v_sub_f32_e32 v110, v110, v158
	v_sub_f32_e32 v111, v111, v158
	v_sub_f32_e32 v112, v112, v158
	v_sub_f32_e32 v113, v113, v158
	v_sub_f32_e32 v118, v118, v158
	v_sub_f32_e32 v119, v119, v158
	v_sub_f32_e32 v120, v120, v158
	v_sub_f32_e32 v121, v121, v158
	v_sub_f32_e32 v130, v130, v158
	v_sub_f32_e32 v131, v131, v158
	v_sub_f32_e32 v132, v132, v158
	v_sub_f32_e32 v133, v133, v158
	v_sub_f32_e32 v134, v134, v158
	v_sub_f32_e32 v135, v135, v158
	v_sub_f32_e32 v136, v136, v158
	v_sub_f32_e32 v137, v137, v158
	v_cndmask_b32_e32 v170, 1.0, v169, vcc
	v_mov_b32_e32 v158, v171
	s_andn2_b64 s[46:47], s[46:47], exec
	s_and_b64 s[52:53], s[52:53], exec
	s_andn2_b64 s[44:45], s[44:45], exec
	s_and_b64 s[48:49], s[48:49], exec
	v_pk_mul_f32 v[96:97], v[96:97], v[170:171] op_sel_hi:[1,0]
	v_pk_mul_f32 v[94:95], v[94:95], v[170:171] op_sel_hi:[1,0]
	v_pk_mul_f32 v[92:93], v[92:93], v[170:171] op_sel_hi:[1,0]
	v_pk_mul_f32 v[90:91], v[90:91], v[170:171] op_sel_hi:[1,0]
	v_pk_mul_f32 v[88:89], v[88:89], v[170:171] op_sel_hi:[1,0]
	v_pk_mul_f32 v[86:87], v[86:87], v[170:171] op_sel_hi:[1,0]
	v_pk_mul_f32 v[84:85], v[84:85], v[170:171] op_sel_hi:[1,0]
	v_pk_mul_f32 v[82:83], v[82:83], v[170:171] op_sel_hi:[1,0]
	v_pk_mul_f32 v[80:81], v[80:81], v[170:171] op_sel_hi:[1,0]
	v_pk_mul_f32 v[78:79], v[78:79], v[170:171] op_sel_hi:[1,0]
	v_pk_mul_f32 v[76:77], v[76:77], v[170:171] op_sel_hi:[1,0]
	v_pk_mul_f32 v[74:75], v[74:75], v[170:171] op_sel_hi:[1,0]
	v_pk_mul_f32 v[72:73], v[72:73], v[170:171] op_sel_hi:[1,0]
	v_pk_mul_f32 v[70:71], v[70:71], v[170:171] op_sel_hi:[1,0]
	v_pk_mul_f32 v[68:69], v[68:69], v[170:171] op_sel_hi:[1,0]
	v_pk_mul_f32 v[66:67], v[66:67], v[170:171] op_sel_hi:[1,0]
	v_add_f32_e32 v168, v168, v160
	v_pk_mul_f32 v[144:145], v[144:145], v[170:171]
	v_pk_mul_f32 v[44:45], v[44:45], v[158:159] op_sel_hi:[1,0]
	v_pk_mul_f32 v[42:43], v[42:43], v[158:159] op_sel_hi:[1,0]
	v_pk_mul_f32 v[28:29], v[28:29], v[158:159] op_sel_hi:[1,0]
	v_pk_mul_f32 v[26:27], v[26:27], v[158:159] op_sel_hi:[1,0]
	v_pk_mul_f32 v[24:25], v[24:25], v[158:159] op_sel_hi:[1,0]
	v_pk_mul_f32 v[22:23], v[22:23], v[158:159] op_sel_hi:[1,0]
	v_pk_mul_f32 v[20:21], v[20:21], v[158:159] op_sel_hi:[1,0]
	v_pk_mul_f32 v[18:19], v[18:19], v[158:159] op_sel_hi:[1,0]
	v_pk_mul_f32 v[16:17], v[16:17], v[158:159] op_sel_hi:[1,0]
	v_pk_mul_f32 v[14:15], v[14:15], v[158:159] op_sel_hi:[1,0]
	v_pk_mul_f32 v[4:5], v[4:5], v[158:159] op_sel_hi:[1,0]
	v_pk_mul_f32 v[2:3], v[2:3], v[158:159] op_sel_hi:[1,0]
	v_pk_mul_f32 v[12:13], v[12:13], v[158:159] op_sel_hi:[1,0]
	v_pk_mul_f32 v[10:11], v[10:11], v[158:159] op_sel_hi:[1,0]
	v_pk_mul_f32 v[8:9], v[8:9], v[158:159] op_sel_hi:[1,0]
	v_pk_mul_f32 v[6:7], v[6:7], v[158:159] op_sel_hi:[1,0]
	v_sub_f32_e32 v106, v106, v160
	v_sub_f32_e32 v107, v107, v160
	v_sub_f32_e32 v108, v108, v160
	v_sub_f32_e32 v109, v109, v160
	v_sub_f32_e32 v114, v114, v160
	v_sub_f32_e32 v115, v115, v160
	v_sub_f32_e32 v116, v116, v160
	v_sub_f32_e32 v117, v117, v160
	v_sub_f32_e32 v122, v122, v160
	v_sub_f32_e32 v123, v123, v160
	v_sub_f32_e32 v124, v124, v160
	v_sub_f32_e32 v125, v125, v160
	v_sub_f32_e32 v126, v126, v160
	v_sub_f32_e32 v127, v127, v160
	v_sub_f32_e32 v128, v128, v160
	v_sub_f32_e32 v129, v129, v160
	s_or_b64 s[46:47], s[46:47], s[52:53]
	s_or_b64 s[44:45], s[44:45], s[48:49]
	s_branch .LBB0_413
